# SGU row sum-of-squares: the sixteen 8-lane ds_bpermute butterflies per unit replaced by DPP adds (quad_perm, quad_perm, exact row_shl:4/row_shr:4 pair), f32, same summation tree
# baseline (speedup 1.0000x reference)
.LBB0_456:
	s_mov_b64 s[16:17], s[0:1]
	s_load_dwordx2 s[10:11], s[16:17], 0xd0
	v_mbcnt_lo_u32_b32 v0, -1, 0
	v_mbcnt_hi_u32_b32 v0, -1, v0
	v_mov_b32_e32 v5, v1
	v_add_u32_e32 v87, s67, v0
	s_waitcnt lgkmcnt(0)
	s_add_u32 s14, s10, 0xbc00000
	v_bfe_u32 v0, v87, 3, 3
	v_readfirstlane_b32 s4, v87
	v_lshl_add_u64 v[2:3], s[8:9], 0, v[0:1]
	s_addc_u32 s15, s11, 0
	s_and_b32 s6, s4, 0xffffffc0
	v_lshlrev_b64 v[2:3], 11, v[2:3]
	v_and_b32_e32 v144, 7, v87
	s_ashr_i32 s7, s6, 31
	v_lshl_add_u64 v[2:3], s[14:15], 0, v[2:3]
	v_lshlrev_b32_e32 v4, 4, v144
	v_lshl_add_u64 v[2:3], s[6:7], 1, v[2:3]
	v_lshl_add_u64 v[2:3], v[2:3], 0, v[4:5]
	s_mov_b32 s5, 0xfffc5000
	v_add_co_u32_e32 v4, vcc, s5, v2
	s_mov_b32 s5, 0xfffc9000
	s_nop 0
	v_addc_co_u32_e32 v5, vcc, -1, v3, vcc
	global_load_dwordx4 v[62:65], v[4:5], off offset:-3072
	v_add_co_u32_e32 v4, vcc, s5, v2
	s_mov_b32 s5, 0xfffcd000
	s_nop 0
	v_addc_co_u32_e32 v5, vcc, -1, v3, vcc
	v_add_co_u32_e32 v6, vcc, s5, v2
	s_mov_b32 s5, 0xfffd1000
	s_nop 0
	v_addc_co_u32_e32 v7, vcc, -1, v3, vcc
	global_load_dwordx4 v[58:61], v[4:5], off offset:-3072
	global_load_dwordx4 v[54:57], v[6:7], off offset:-3072
	v_add_co_u32_e32 v4, vcc, s5, v2
	s_mov_b32 s5, 0xfffd5000
	s_nop 0
	v_addc_co_u32_e32 v5, vcc, -1, v3, vcc
	v_add_co_u32_e32 v6, vcc, s5, v2
	s_mov_b32 s5, 0xfffd9000
	s_nop 0
	v_addc_co_u32_e32 v7, vcc, -1, v3, vcc
	global_load_dwordx4 v[50:53], v[4:5], off offset:-3072
	global_load_dwordx4 v[46:49], v[6:7], off offset:-3072
	v_add_co_u32_e32 v4, vcc, s5, v2
	s_mov_b32 s5, 0xfffdd000
	s_nop 0
	v_addc_co_u32_e32 v5, vcc, -1, v3, vcc
	v_add_co_u32_e32 v6, vcc, s5, v2
	s_mov_b32 s5, 0xfffe1000
	s_nop 0
	v_addc_co_u32_e32 v7, vcc, -1, v3, vcc
	global_load_dwordx4 v[42:45], v[4:5], off offset:-3072
	global_load_dwordx4 v[38:41], v[6:7], off offset:-3072
	v_add_co_u32_e32 v4, vcc, s5, v2
	s_mov_b32 s5, 0xfffe5000
	s_nop 0
	v_addc_co_u32_e32 v5, vcc, -1, v3, vcc
	v_add_co_u32_e32 v6, vcc, s5, v2
	s_mov_b32 s5, 0xfffe9000
	s_nop 0
	v_addc_co_u32_e32 v7, vcc, -1, v3, vcc
	global_load_dwordx4 v[34:37], v[4:5], off offset:-3072
	global_load_dwordx4 v[30:33], v[6:7], off offset:-3072
	v_add_co_u32_e32 v4, vcc, s5, v2
	s_mov_b32 s5, 0xfffed000
	s_nop 0
	v_addc_co_u32_e32 v5, vcc, -1, v3, vcc
	v_add_co_u32_e32 v6, vcc, s5, v2
	s_mov_b32 s5, 0xffff1000
	s_nop 0
	v_addc_co_u32_e32 v7, vcc, -1, v3, vcc
	global_load_dwordx4 v[26:29], v[4:5], off offset:-3072
	global_load_dwordx4 v[22:25], v[6:7], off offset:-3072
	v_add_co_u32_e32 v4, vcc, s5, v2
	s_mov_b32 s5, 0xffff5000
	s_nop 0
	v_addc_co_u32_e32 v5, vcc, -1, v3, vcc
	v_add_co_u32_e32 v6, vcc, s5, v2
	s_movk_i32 s5, 0x9000
	s_nop 0
	v_addc_co_u32_e32 v7, vcc, -1, v3, vcc
	global_load_dwordx4 v[18:21], v[4:5], off offset:-3072
	global_load_dwordx4 v[14:17], v[6:7], off offset:-3072
	v_add_co_u32_e32 v4, vcc, s5, v2
	s_movk_i32 s5, 0xd000
	s_nop 0
	v_addc_co_u32_e32 v5, vcc, -1, v3, vcc
	v_add_co_u32_e32 v6, vcc, s5, v2
	v_and_b32_e32 v67, 64, v234
	s_nop 0
	v_addc_co_u32_e32 v7, vcc, -1, v3, vcc
	global_load_dwordx4 v[10:13], v[4:5], off offset:-3072
	s_nop 0
	global_load_dwordx4 v[6:9], v[6:7], off offset:-3072
	s_nop 0
	global_load_dwordx4 v[2:5], v[2:3], off offset:1024
	v_xor_b32_e32 v66, 1, v234
	v_add_u32_e32 v104, 64, v67
	s_waitcnt vmcnt(0)
	v_and_b32_e32 v151, 0xffff0000, v62
	v_and_b32_e32 v153, 0xffff0000, v63
	v_lshlrev_b32_e32 v152, 16, v62
	v_mul_f32_e32 v62, v151, v151
	v_lshlrev_b32_e32 v154, 16, v63
	v_mul_f32_e32 v63, v153, v153
	v_fmac_f32_e32 v62, v152, v152
	v_fmac_f32_e32 v63, v154, v154
	v_and_b32_e32 v155, 0xffff0000, v64
	v_add_f32_e32 v62, v62, v63
	v_lshlrev_b32_e32 v156, 16, v64
	v_mul_f32_e32 v63, v155, v155
	v_fmac_f32_e32 v63, v156, v156
	v_and_b32_e32 v157, 0xffff0000, v65
	v_cmp_lt_i32_e32 vcc, v66, v104
	v_add_f32_e32 v62, v63, v62
	v_lshlrev_b32_e32 v158, 16, v65
	v_mul_f32_e32 v63, v157, v157
	v_cndmask_b32_e32 v66, v234, v66, vcc
	v_fmac_f32_e32 v63, v158, v158
	v_lshlrev_b32_e32 v102, 2, v66
	v_add_f32_e32 v62, v63, v62
	s_nop 1
	v_add_f32_dpp v62, v62, v62 quad_perm:[1,0,3,2] row_mask:0xf bank_mask:0xf
	s_nop 1
	v_add_f32_dpp v62, v62, v62 quad_perm:[2,3,0,1] row_mask:0xf bank_mask:0xf
	s_nop 1
	v_mov_b32_e32 v63, v62
	s_nop 1
	v_add_f32_dpp v62, v63, v62 row_shl:4 row_mask:0xf bank_mask:0x5
	s_nop 1
	v_add_f32_dpp v62, v63, v62 row_shr:4 row_mask:0xf bank_mask:0xa
	s_nop 1
	v_mov_b32_e32 v63, 0
	v_xor_b32_e32 v66, 2, v234
	v_cmp_lt_i32_e32 vcc, v66, v104
	s_ashr_i32 s12, s4, 6
	s_lshl_b32 s4, s12, 2
	v_cndmask_b32_e32 v64, v234, v66, vcc
	v_lshlrev_b32_e32 v101, 2, v64
	s_waitcnt lgkmcnt(0)
	v_add_f32_e32 v62, v62, v63
	v_mov_b32_e32 v63, 0
	v_xor_b32_e32 v64, 4, v234
	v_cmp_lt_i32_e32 vcc, v64, v104
	s_add_i32 s4, s4, 0
	s_add_i32 s4, s4, 0x22000
	v_cndmask_b32_e32 v64, v234, v64, vcc
	v_lshlrev_b32_e32 v100, 2, v64
	s_waitcnt lgkmcnt(0)
	v_add_f32_e32 v62, v62, v63
	v_mov_b32_e32 v63, 0
	v_and_b32_e32 v64, 56, v87
	v_cmp_eq_u32_e32 vcc, 0, v144
	v_lshl_add_u32 v103, v64, 2, s4
	s_and_saveexec_b64 s[18:19], vcc
	s_cbranch_execz .LBB0_458
	s_waitcnt lgkmcnt(0)
	v_add_f32_e32 v62, v62, v63
	ds_write_b32 v103, v62
.LBB0_458:
	s_or_b64 exec, exec, s[18:19]
	v_and_b32_e32 v135, 0xffff0000, v58
	v_and_b32_e32 v137, 0xffff0000, v59
	v_lshlrev_b32_e32 v136, 16, v58
	v_mul_f32_e32 v58, v135, v135
	v_lshlrev_b32_e32 v138, 16, v59
	v_mul_f32_e32 v59, v137, v137
	v_fmac_f32_e32 v58, v136, v136
	v_fmac_f32_e32 v59, v138, v138
	v_and_b32_e32 v139, 0xffff0000, v60
	v_add_f32_e32 v58, v58, v59
	v_lshlrev_b32_e32 v140, 16, v60
	v_mul_f32_e32 v59, v139, v139
	v_fmac_f32_e32 v59, v140, v140
	v_and_b32_e32 v141, 0xffff0000, v61
	v_add_f32_e32 v58, v59, v58
	v_lshlrev_b32_e32 v142, 16, v61
	v_mul_f32_e32 v59, v141, v141
	v_fmac_f32_e32 v59, v142, v142
	v_add_f32_e32 v58, v59, v58
	s_nop 1
	v_add_f32_dpp v58, v58, v58 quad_perm:[1,0,3,2] row_mask:0xf bank_mask:0xf
	s_nop 1
	v_add_f32_dpp v58, v58, v58 quad_perm:[2,3,0,1] row_mask:0xf bank_mask:0xf
	s_nop 1
	v_mov_b32_e32 v59, v58
	s_nop 1
	v_add_f32_dpp v58, v59, v58 row_shl:4 row_mask:0xf bank_mask:0x5
	s_nop 1
	v_add_f32_dpp v58, v59, v58 row_shr:4 row_mask:0xf bank_mask:0xa
	s_nop 1
	v_mov_b32_e32 v59, 0
	s_load_dwordx2 s[18:19], s[16:17], 0x30
	s_nop 0
	s_load_dwordx2 s[16:17], s[16:17], 0x40
	s_waitcnt lgkmcnt(0)
	v_add_f32_e32 v58, v58, v59
	v_mov_b32_e32 v59, 0
	s_waitcnt lgkmcnt(0)
	v_add_f32_e32 v58, v58, v59
	v_mov_b32_e32 v59, 0
	s_and_saveexec_b64 s[20:21], vcc
	s_cbranch_execz .LBB0_460
	s_waitcnt lgkmcnt(0)
	v_add_f32_e32 v58, v58, v59
	ds_write_b32 v103, v58 offset:256
.LBB0_460:
	s_or_b64 exec, exec, s[20:21]
	v_and_b32_e32 v123, 0xffff0000, v54
	v_and_b32_e32 v125, 0xffff0000, v55
	v_lshlrev_b32_e32 v124, 16, v54
	v_mul_f32_e32 v54, v123, v123
	v_lshlrev_b32_e32 v126, 16, v55
	v_mul_f32_e32 v55, v125, v125
	v_fmac_f32_e32 v54, v124, v124
	v_fmac_f32_e32 v55, v126, v126
	v_and_b32_e32 v127, 0xffff0000, v56
	v_add_f32_e32 v54, v54, v55
	v_lshlrev_b32_e32 v129, 16, v56
	v_mul_f32_e32 v55, v127, v127
	v_fmac_f32_e32 v55, v129, v129
	v_and_b32_e32 v130, 0xffff0000, v57
	v_add_f32_e32 v54, v55, v54
	v_lshlrev_b32_e32 v131, 16, v57
	v_mul_f32_e32 v55, v130, v130
	v_fmac_f32_e32 v55, v131, v131
	v_add_f32_e32 v54, v55, v54
	s_nop 1
	v_add_f32_dpp v54, v54, v54 quad_perm:[1,0,3,2] row_mask:0xf bank_mask:0xf
	s_nop 1
	v_add_f32_dpp v54, v54, v54 quad_perm:[2,3,0,1] row_mask:0xf bank_mask:0xf
	s_nop 1
	v_mov_b32_e32 v55, v54
	s_nop 1
	v_add_f32_dpp v54, v55, v54 row_shl:4 row_mask:0xf bank_mask:0x5
	s_nop 1
	v_add_f32_dpp v54, v55, v54 row_shr:4 row_mask:0xf bank_mask:0xa
	s_nop 1
	v_mov_b32_e32 v55, 0
	s_waitcnt lgkmcnt(0)
	v_add_f32_e32 v54, v54, v55
	v_mov_b32_e32 v55, 0
	s_waitcnt lgkmcnt(0)
	v_add_f32_e32 v54, v54, v55
	v_mov_b32_e32 v55, 0
	s_and_saveexec_b64 s[20:21], vcc
	s_cbranch_execz .LBB0_462
	s_waitcnt lgkmcnt(0)
	v_add_f32_e32 v54, v54, v55
	ds_write_b32 v103, v54 offset:512
.LBB0_462:
	s_or_b64 exec, exec, s[20:21]
	v_and_b32_e32 v115, 0xffff0000, v50
	v_and_b32_e32 v117, 0xffff0000, v51
	v_lshlrev_b32_e32 v116, 16, v50
	v_mul_f32_e32 v50, v115, v115
	v_lshlrev_b32_e32 v118, 16, v51
	v_mul_f32_e32 v51, v117, v117
	v_fmac_f32_e32 v50, v116, v116
	v_fmac_f32_e32 v51, v118, v118
	v_and_b32_e32 v119, 0xffff0000, v52
	v_add_f32_e32 v50, v50, v51
	v_lshlrev_b32_e32 v120, 16, v52
	v_mul_f32_e32 v51, v119, v119
	v_fmac_f32_e32 v51, v120, v120
	v_and_b32_e32 v121, 0xffff0000, v53
	v_add_f32_e32 v50, v51, v50
	v_lshlrev_b32_e32 v122, 16, v53
	v_mul_f32_e32 v51, v121, v121
	v_fmac_f32_e32 v51, v122, v122
	v_add_f32_e32 v50, v51, v50
	s_nop 1
	v_add_f32_dpp v50, v50, v50 quad_perm:[1,0,3,2] row_mask:0xf bank_mask:0xf
	s_nop 1
	v_add_f32_dpp v50, v50, v50 quad_perm:[2,3,0,1] row_mask:0xf bank_mask:0xf
	s_nop 1
	v_mov_b32_e32 v51, v50
	s_nop 1
	v_add_f32_dpp v50, v51, v50 row_shl:4 row_mask:0xf bank_mask:0x5
	s_nop 1
	v_add_f32_dpp v50, v51, v50 row_shr:4 row_mask:0xf bank_mask:0xa
	s_nop 1
	v_mov_b32_e32 v51, 0
	s_waitcnt lgkmcnt(0)
	v_add_f32_e32 v50, v50, v51
	v_mov_b32_e32 v51, 0
	s_waitcnt lgkmcnt(0)
	v_add_f32_e32 v50, v50, v51
	v_mov_b32_e32 v51, 0
	s_and_saveexec_b64 s[20:21], vcc
	s_cbranch_execz .LBB0_464
	s_waitcnt lgkmcnt(0)
	v_add_f32_e32 v50, v50, v51
	ds_write_b32 v103, v50 offset:768
.LBB0_464:
	s_or_b64 exec, exec, s[20:21]
	v_and_b32_e32 v107, 0xffff0000, v46
	v_and_b32_e32 v109, 0xffff0000, v47
	v_lshlrev_b32_e32 v108, 16, v46
	v_mul_f32_e32 v46, v107, v107
	v_lshlrev_b32_e32 v110, 16, v47
	v_mul_f32_e32 v47, v109, v109
	v_fmac_f32_e32 v46, v108, v108
	v_fmac_f32_e32 v47, v110, v110
	v_and_b32_e32 v111, 0xffff0000, v48
	v_add_f32_e32 v46, v46, v47
	v_lshlrev_b32_e32 v112, 16, v48
	v_mul_f32_e32 v47, v111, v111
	v_fmac_f32_e32 v47, v112, v112
	v_and_b32_e32 v113, 0xffff0000, v49
	v_add_f32_e32 v46, v47, v46
	v_lshlrev_b32_e32 v114, 16, v49
	v_mul_f32_e32 v47, v113, v113
	v_fmac_f32_e32 v47, v114, v114
	v_add_f32_e32 v46, v47, v46
	s_nop 1
	v_add_f32_dpp v46, v46, v46 quad_perm:[1,0,3,2] row_mask:0xf bank_mask:0xf
	s_nop 1
	v_add_f32_dpp v46, v46, v46 quad_perm:[2,3,0,1] row_mask:0xf bank_mask:0xf
	s_nop 1
	v_mov_b32_e32 v47, v46
	s_nop 1
	v_add_f32_dpp v46, v47, v46 row_shl:4 row_mask:0xf bank_mask:0x5
	s_nop 1
	v_add_f32_dpp v46, v47, v46 row_shr:4 row_mask:0xf bank_mask:0xa
	s_nop 1
	v_mov_b32_e32 v47, 0
	s_waitcnt lgkmcnt(0)
	v_add_f32_e32 v46, v46, v47
	v_mov_b32_e32 v47, 0
	s_waitcnt lgkmcnt(0)
	v_add_f32_e32 v46, v46, v47
	v_mov_b32_e32 v47, 0
	s_and_saveexec_b64 s[20:21], vcc
	s_cbranch_execz .LBB0_466
	s_waitcnt lgkmcnt(0)
	v_add_f32_e32 v46, v46, v47
	ds_write_b32 v103, v46 offset:1024
.LBB0_466:
	s_or_b64 exec, exec, s[20:21]
	v_and_b32_e32 v92, 0xffff0000, v42
	v_and_b32_e32 v94, 0xffff0000, v43
	v_lshlrev_b32_e32 v93, 16, v42
	v_mul_f32_e32 v42, v92, v92
	v_lshlrev_b32_e32 v95, 16, v43
	v_mul_f32_e32 v43, v94, v94
	v_fmac_f32_e32 v42, v93, v93
	v_fmac_f32_e32 v43, v95, v95
	v_and_b32_e32 v96, 0xffff0000, v44
	v_add_f32_e32 v42, v42, v43
	v_lshlrev_b32_e32 v97, 16, v44
	v_mul_f32_e32 v43, v96, v96
	v_fmac_f32_e32 v43, v97, v97
	v_and_b32_e32 v98, 0xffff0000, v45
	v_add_f32_e32 v42, v43, v42
	v_lshlrev_b32_e32 v99, 16, v45
	v_mul_f32_e32 v43, v98, v98
	v_fmac_f32_e32 v43, v99, v99
	v_add_f32_e32 v42, v43, v42
	s_nop 1
	v_add_f32_dpp v42, v42, v42 quad_perm:[1,0,3,2] row_mask:0xf bank_mask:0xf
	s_nop 1
	v_add_f32_dpp v42, v42, v42 quad_perm:[2,3,0,1] row_mask:0xf bank_mask:0xf
	s_nop 1
	v_mov_b32_e32 v43, v42
	s_nop 1
	v_add_f32_dpp v42, v43, v42 row_shl:4 row_mask:0xf bank_mask:0x5
	s_nop 1
	v_add_f32_dpp v42, v43, v42 row_shr:4 row_mask:0xf bank_mask:0xa
	s_nop 1
	v_mov_b32_e32 v43, 0
	s_waitcnt lgkmcnt(0)
	v_add_f32_e32 v42, v42, v43
	v_mov_b32_e32 v43, 0
	s_waitcnt lgkmcnt(0)
	v_add_f32_e32 v42, v42, v43
	v_mov_b32_e32 v43, 0
	s_and_saveexec_b64 s[20:21], vcc
	s_cbranch_execz .LBB0_468
	s_waitcnt lgkmcnt(0)
	v_add_f32_e32 v42, v42, v43
	ds_write_b32 v103, v42 offset:1280
.LBB0_468:
	s_or_b64 exec, exec, s[20:21]
	v_and_b32_e32 v83, 0xffff0000, v38
	v_and_b32_e32 v85, 0xffff0000, v39
	v_lshlrev_b32_e32 v84, 16, v38
	v_mul_f32_e32 v38, v83, v83
	v_lshlrev_b32_e32 v86, 16, v39
	v_mul_f32_e32 v39, v85, v85
	v_fmac_f32_e32 v38, v84, v84
	v_fmac_f32_e32 v39, v86, v86
	v_and_b32_e32 v88, 0xffff0000, v40
	v_add_f32_e32 v38, v38, v39
	v_lshlrev_b32_e32 v89, 16, v40
	v_mul_f32_e32 v39, v88, v88
	v_fmac_f32_e32 v39, v89, v89
	v_and_b32_e32 v90, 0xffff0000, v41
	v_add_f32_e32 v38, v39, v38
	v_lshlrev_b32_e32 v91, 16, v41
	v_mul_f32_e32 v39, v90, v90
	v_fmac_f32_e32 v39, v91, v91
	v_add_f32_e32 v38, v39, v38
	s_nop 1
	v_add_f32_dpp v38, v38, v38 quad_perm:[1,0,3,2] row_mask:0xf bank_mask:0xf
	s_nop 1
	v_add_f32_dpp v38, v38, v38 quad_perm:[2,3,0,1] row_mask:0xf bank_mask:0xf
	s_nop 1
	v_mov_b32_e32 v39, v38
	s_nop 1
	v_add_f32_dpp v38, v39, v38 row_shl:4 row_mask:0xf bank_mask:0x5
	s_nop 1
	v_add_f32_dpp v38, v39, v38 row_shr:4 row_mask:0xf bank_mask:0xa
	s_nop 1
	v_mov_b32_e32 v39, 0
	s_waitcnt lgkmcnt(0)
	v_add_f32_e32 v38, v38, v39
	v_mov_b32_e32 v39, 0
	s_waitcnt lgkmcnt(0)
	v_add_f32_e32 v38, v38, v39
	v_mov_b32_e32 v39, 0
	s_and_saveexec_b64 s[20:21], vcc
	s_cbranch_execz .LBB0_470
	s_waitcnt lgkmcnt(0)
	v_add_f32_e32 v38, v38, v39
	ds_write_b32 v103, v38 offset:1536
.LBB0_470:
	s_or_b64 exec, exec, s[20:21]
	v_and_b32_e32 v75, 0xffff0000, v34
	v_and_b32_e32 v77, 0xffff0000, v35
	v_lshlrev_b32_e32 v76, 16, v34
	v_mul_f32_e32 v34, v75, v75
	v_lshlrev_b32_e32 v78, 16, v35
	v_mul_f32_e32 v35, v77, v77
	v_fmac_f32_e32 v34, v76, v76
	v_fmac_f32_e32 v35, v78, v78
	v_and_b32_e32 v79, 0xffff0000, v36
	v_add_f32_e32 v34, v34, v35
	v_lshlrev_b32_e32 v80, 16, v36
	v_mul_f32_e32 v35, v79, v79
	v_fmac_f32_e32 v35, v80, v80
	v_and_b32_e32 v81, 0xffff0000, v37
	v_add_f32_e32 v34, v35, v34
	v_lshlrev_b32_e32 v82, 16, v37
	v_mul_f32_e32 v35, v81, v81
	v_fmac_f32_e32 v35, v82, v82
	v_add_f32_e32 v34, v35, v34
	s_nop 1
	v_add_f32_dpp v34, v34, v34 quad_perm:[1,0,3,2] row_mask:0xf bank_mask:0xf
	s_nop 1
	v_add_f32_dpp v34, v34, v34 quad_perm:[2,3,0,1] row_mask:0xf bank_mask:0xf
	s_nop 1
	v_mov_b32_e32 v35, v34
	s_nop 1
	v_add_f32_dpp v34, v35, v34 row_shl:4 row_mask:0xf bank_mask:0x5
	s_nop 1
	v_add_f32_dpp v34, v35, v34 row_shr:4 row_mask:0xf bank_mask:0xa
	s_nop 1
	v_mov_b32_e32 v35, 0
	s_waitcnt lgkmcnt(0)
	v_add_f32_e32 v34, v34, v35
	v_mov_b32_e32 v35, 0
	s_waitcnt lgkmcnt(0)
	v_add_f32_e32 v34, v34, v35
	v_mov_b32_e32 v35, 0
	s_and_saveexec_b64 s[20:21], vcc
	s_cbranch_execz .LBB0_472
	s_waitcnt lgkmcnt(0)
	v_add_f32_e32 v34, v34, v35
	ds_write_b32 v103, v34 offset:1792
.LBB0_472:
	s_or_b64 exec, exec, s[20:21]
	v_and_b32_e32 v67, 0xffff0000, v30
	v_and_b32_e32 v69, 0xffff0000, v31
	v_lshlrev_b32_e32 v68, 16, v30
	v_mul_f32_e32 v30, v67, v67
	v_lshlrev_b32_e32 v70, 16, v31
	v_mul_f32_e32 v31, v69, v69
	v_fmac_f32_e32 v30, v68, v68
	v_fmac_f32_e32 v31, v70, v70
	v_and_b32_e32 v71, 0xffff0000, v32
	v_add_f32_e32 v30, v30, v31
	v_lshlrev_b32_e32 v72, 16, v32
	v_mul_f32_e32 v31, v71, v71
	v_fmac_f32_e32 v31, v72, v72
	v_and_b32_e32 v73, 0xffff0000, v33
	v_add_f32_e32 v30, v31, v30
	v_lshlrev_b32_e32 v74, 16, v33
	v_mul_f32_e32 v31, v73, v73
	v_fmac_f32_e32 v31, v74, v74
	v_add_f32_e32 v30, v31, v30
	s_nop 1
	v_add_f32_dpp v30, v30, v30 quad_perm:[1,0,3,2] row_mask:0xf bank_mask:0xf
	s_nop 1
	v_add_f32_dpp v30, v30, v30 quad_perm:[2,3,0,1] row_mask:0xf bank_mask:0xf
	s_nop 1
	v_mov_b32_e32 v31, v30
	s_nop 1
	v_add_f32_dpp v30, v31, v30 row_shl:4 row_mask:0xf bank_mask:0x5
	s_nop 1
	v_add_f32_dpp v30, v31, v30 row_shr:4 row_mask:0xf bank_mask:0xa
	s_nop 1
	v_mov_b32_e32 v31, 0
	s_waitcnt lgkmcnt(0)
	v_add_f32_e32 v30, v30, v31
	v_mov_b32_e32 v31, 0
	s_waitcnt lgkmcnt(0)
	v_add_f32_e32 v30, v30, v31
	v_mov_b32_e32 v31, 0
	s_and_saveexec_b64 s[20:21], vcc
	s_cbranch_execz .LBB0_474
	s_waitcnt lgkmcnt(0)
	v_add_f32_e32 v30, v30, v31
	ds_write_b32 v103, v30 offset:2048
.LBB0_474:
	s_or_b64 exec, exec, s[20:21]
	v_and_b32_e32 v59, 0xffff0000, v26
	v_and_b32_e32 v61, 0xffff0000, v27
	v_lshlrev_b32_e32 v60, 16, v26
	v_mul_f32_e32 v26, v59, v59
	v_lshlrev_b32_e32 v62, 16, v27
	v_mul_f32_e32 v27, v61, v61
	v_fmac_f32_e32 v26, v60, v60
	v_fmac_f32_e32 v27, v62, v62
	v_and_b32_e32 v63, 0xffff0000, v28
	v_add_f32_e32 v26, v26, v27
	v_lshlrev_b32_e32 v64, 16, v28
	v_mul_f32_e32 v27, v63, v63
	v_fmac_f32_e32 v27, v64, v64
	v_and_b32_e32 v65, 0xffff0000, v29
	v_add_f32_e32 v26, v27, v26
	v_lshlrev_b32_e32 v66, 16, v29
	v_mul_f32_e32 v27, v65, v65
	v_fmac_f32_e32 v27, v66, v66
	v_add_f32_e32 v26, v27, v26
	s_nop 1
	v_add_f32_dpp v26, v26, v26 quad_perm:[1,0,3,2] row_mask:0xf bank_mask:0xf
	s_nop 1
	v_add_f32_dpp v26, v26, v26 quad_perm:[2,3,0,1] row_mask:0xf bank_mask:0xf
	s_nop 1
	v_mov_b32_e32 v27, v26
	s_nop 1
	v_add_f32_dpp v26, v27, v26 row_shl:4 row_mask:0xf bank_mask:0x5
	s_nop 1
	v_add_f32_dpp v26, v27, v26 row_shr:4 row_mask:0xf bank_mask:0xa
	s_nop 1
	v_mov_b32_e32 v27, 0
	s_waitcnt lgkmcnt(0)
	v_add_f32_e32 v26, v26, v27
	v_mov_b32_e32 v27, 0
	s_waitcnt lgkmcnt(0)
	v_add_f32_e32 v26, v26, v27
	v_mov_b32_e32 v27, 0
	s_and_saveexec_b64 s[20:21], vcc
	s_cbranch_execz .LBB0_476
	s_waitcnt lgkmcnt(0)
	v_add_f32_e32 v26, v26, v27
	ds_write_b32 v103, v26 offset:2304
.LBB0_476:
	s_or_b64 exec, exec, s[20:21]
	v_and_b32_e32 v51, 0xffff0000, v22
	v_and_b32_e32 v53, 0xffff0000, v23
	v_lshlrev_b32_e32 v52, 16, v22
	v_mul_f32_e32 v22, v51, v51
	v_lshlrev_b32_e32 v54, 16, v23
	v_mul_f32_e32 v23, v53, v53
	v_fmac_f32_e32 v22, v52, v52
	v_fmac_f32_e32 v23, v54, v54
	v_and_b32_e32 v55, 0xffff0000, v24
	v_add_f32_e32 v22, v22, v23
	v_lshlrev_b32_e32 v56, 16, v24
	v_mul_f32_e32 v23, v55, v55
	v_fmac_f32_e32 v23, v56, v56
	v_and_b32_e32 v57, 0xffff0000, v25
	v_add_f32_e32 v22, v23, v22
	v_lshlrev_b32_e32 v58, 16, v25
	v_mul_f32_e32 v23, v57, v57
	v_fmac_f32_e32 v23, v58, v58
	v_add_f32_e32 v22, v23, v22
	s_nop 1
	v_add_f32_dpp v22, v22, v22 quad_perm:[1,0,3,2] row_mask:0xf bank_mask:0xf
	s_nop 1
	v_add_f32_dpp v22, v22, v22 quad_perm:[2,3,0,1] row_mask:0xf bank_mask:0xf
	s_nop 1
	v_mov_b32_e32 v23, v22
	s_nop 1
	v_add_f32_dpp v22, v23, v22 row_shl:4 row_mask:0xf bank_mask:0x5
	s_nop 1
	v_add_f32_dpp v22, v23, v22 row_shr:4 row_mask:0xf bank_mask:0xa
	s_nop 1
	v_mov_b32_e32 v23, 0
	s_waitcnt lgkmcnt(0)
	v_add_f32_e32 v22, v22, v23
	v_mov_b32_e32 v23, 0
	s_waitcnt lgkmcnt(0)
	v_add_f32_e32 v22, v22, v23
	v_mov_b32_e32 v23, 0
	s_and_saveexec_b64 s[20:21], vcc
	s_cbranch_execz .LBB0_478
	s_waitcnt lgkmcnt(0)
	v_add_f32_e32 v22, v22, v23
	ds_write_b32 v103, v22 offset:2560
.LBB0_478:
	s_or_b64 exec, exec, s[20:21]
	v_and_b32_e32 v42, 0xffff0000, v18
	v_and_b32_e32 v44, 0xffff0000, v19
	v_lshlrev_b32_e32 v43, 16, v18
	v_mul_f32_e32 v18, v42, v42
	v_lshlrev_b32_e32 v45, 16, v19
	v_mul_f32_e32 v19, v44, v44
	v_fmac_f32_e32 v18, v43, v43
	v_fmac_f32_e32 v19, v45, v45
	v_and_b32_e32 v46, 0xffff0000, v20
	v_add_f32_e32 v18, v18, v19
	v_lshlrev_b32_e32 v47, 16, v20
	v_mul_f32_e32 v19, v46, v46
	v_fmac_f32_e32 v19, v47, v47
	v_and_b32_e32 v48, 0xffff0000, v21
	v_add_f32_e32 v18, v19, v18
	v_lshlrev_b32_e32 v50, 16, v21
	v_mul_f32_e32 v19, v48, v48
	v_fmac_f32_e32 v19, v50, v50
	v_add_f32_e32 v18, v19, v18
	s_nop 1
	v_add_f32_dpp v18, v18, v18 quad_perm:[1,0,3,2] row_mask:0xf bank_mask:0xf
	s_nop 1
	v_add_f32_dpp v18, v18, v18 quad_perm:[2,3,0,1] row_mask:0xf bank_mask:0xf
	s_nop 1
	v_mov_b32_e32 v19, v18
	s_nop 1
	v_add_f32_dpp v18, v19, v18 row_shl:4 row_mask:0xf bank_mask:0x5
	s_nop 1
	v_add_f32_dpp v18, v19, v18 row_shr:4 row_mask:0xf bank_mask:0xa
	s_nop 1
	v_mov_b32_e32 v19, 0
	s_waitcnt lgkmcnt(0)
	v_add_f32_e32 v18, v18, v19
	v_mov_b32_e32 v19, 0
	s_waitcnt lgkmcnt(0)
	v_add_f32_e32 v18, v18, v19
	v_mov_b32_e32 v19, 0
	s_and_saveexec_b64 s[20:21], vcc
	s_cbranch_execz .LBB0_480
	s_waitcnt lgkmcnt(0)
	v_add_f32_e32 v18, v18, v19
	ds_write_b32 v103, v18 offset:2816
.LBB0_480:
	s_or_b64 exec, exec, s[20:21]
	v_and_b32_e32 v34, 0xffff0000, v14
	v_and_b32_e32 v36, 0xffff0000, v15
	v_lshlrev_b32_e32 v35, 16, v14
	v_mul_f32_e32 v14, v34, v34
	v_lshlrev_b32_e32 v37, 16, v15
	v_mul_f32_e32 v15, v36, v36
	v_fmac_f32_e32 v14, v35, v35
	v_fmac_f32_e32 v15, v37, v37
	v_and_b32_e32 v38, 0xffff0000, v16
	v_add_f32_e32 v14, v14, v15
	v_lshlrev_b32_e32 v39, 16, v16
	v_mul_f32_e32 v15, v38, v38
	v_fmac_f32_e32 v15, v39, v39
	v_and_b32_e32 v40, 0xffff0000, v17
	v_add_f32_e32 v14, v15, v14
	v_lshlrev_b32_e32 v41, 16, v17
	v_mul_f32_e32 v15, v40, v40
	v_fmac_f32_e32 v15, v41, v41
	v_add_f32_e32 v14, v15, v14
	s_nop 1
	v_add_f32_dpp v14, v14, v14 quad_perm:[1,0,3,2] row_mask:0xf bank_mask:0xf
	s_nop 1
	v_add_f32_dpp v14, v14, v14 quad_perm:[2,3,0,1] row_mask:0xf bank_mask:0xf
	s_nop 1
	v_mov_b32_e32 v15, v14
	s_nop 1
	v_add_f32_dpp v14, v15, v14 row_shl:4 row_mask:0xf bank_mask:0x5
	s_nop 1
	v_add_f32_dpp v14, v15, v14 row_shr:4 row_mask:0xf bank_mask:0xa
	s_nop 1
	v_mov_b32_e32 v15, 0
	s_waitcnt lgkmcnt(0)
	v_add_f32_e32 v14, v14, v15
	v_mov_b32_e32 v15, 0
	s_waitcnt lgkmcnt(0)
	v_add_f32_e32 v14, v14, v15
	v_mov_b32_e32 v15, 0
	s_and_saveexec_b64 s[20:21], vcc
	s_cbranch_execz .LBB0_482
	s_waitcnt lgkmcnt(0)
	v_add_f32_e32 v14, v14, v15
	ds_write_b32 v103, v14 offset:3072
.LBB0_482:
	s_or_b64 exec, exec, s[20:21]
	v_and_b32_e32 v26, 0xffff0000, v10
	v_and_b32_e32 v28, 0xffff0000, v11
	v_lshlrev_b32_e32 v27, 16, v10
	v_mul_f32_e32 v10, v26, v26
	v_lshlrev_b32_e32 v29, 16, v11
	v_mul_f32_e32 v11, v28, v28
	v_fmac_f32_e32 v10, v27, v27
	v_fmac_f32_e32 v11, v29, v29
	v_and_b32_e32 v30, 0xffff0000, v12
	v_add_f32_e32 v10, v10, v11
	v_lshlrev_b32_e32 v31, 16, v12
	v_mul_f32_e32 v11, v30, v30
	v_fmac_f32_e32 v11, v31, v31
	v_and_b32_e32 v32, 0xffff0000, v13
	v_add_f32_e32 v10, v11, v10
	v_lshlrev_b32_e32 v33, 16, v13
	v_mul_f32_e32 v11, v32, v32
	v_fmac_f32_e32 v11, v33, v33
	v_add_f32_e32 v10, v11, v10
	s_nop 1
	v_add_f32_dpp v10, v10, v10 quad_perm:[1,0,3,2] row_mask:0xf bank_mask:0xf
	s_nop 1
	v_add_f32_dpp v10, v10, v10 quad_perm:[2,3,0,1] row_mask:0xf bank_mask:0xf
	s_nop 1
	v_mov_b32_e32 v11, v10
	s_nop 1
	v_add_f32_dpp v10, v11, v10 row_shl:4 row_mask:0xf bank_mask:0x5
	s_nop 1
	v_add_f32_dpp v10, v11, v10 row_shr:4 row_mask:0xf bank_mask:0xa
	s_nop 1
	v_mov_b32_e32 v11, 0
	s_waitcnt lgkmcnt(0)
	v_add_f32_e32 v10, v10, v11
	v_mov_b32_e32 v11, 0
	s_waitcnt lgkmcnt(0)
	v_add_f32_e32 v10, v10, v11
	v_mov_b32_e32 v11, 0
	s_and_saveexec_b64 s[20:21], vcc
	s_cbranch_execz .LBB0_484
	s_waitcnt lgkmcnt(0)
	v_add_f32_e32 v10, v10, v11
	ds_write_b32 v103, v10 offset:3328
.LBB0_484:
	s_or_b64 exec, exec, s[20:21]
	v_and_b32_e32 v18, 0xffff0000, v6
	v_and_b32_e32 v20, 0xffff0000, v7
	v_lshlrev_b32_e32 v19, 16, v6
	v_mul_f32_e32 v6, v18, v18
	v_lshlrev_b32_e32 v21, 16, v7
	v_mul_f32_e32 v7, v20, v20
	v_fmac_f32_e32 v6, v19, v19
	v_fmac_f32_e32 v7, v21, v21
	v_and_b32_e32 v22, 0xffff0000, v8
	v_add_f32_e32 v6, v6, v7
	v_lshlrev_b32_e32 v23, 16, v8
	v_mul_f32_e32 v7, v22, v22
	v_fmac_f32_e32 v7, v23, v23
	v_and_b32_e32 v24, 0xffff0000, v9
	v_add_f32_e32 v6, v7, v6
	v_lshlrev_b32_e32 v25, 16, v9
	v_mul_f32_e32 v7, v24, v24
	v_fmac_f32_e32 v7, v25, v25
	v_add_f32_e32 v6, v7, v6
	s_nop 1
	v_add_f32_dpp v6, v6, v6 quad_perm:[1,0,3,2] row_mask:0xf bank_mask:0xf
	s_nop 1
	v_add_f32_dpp v6, v6, v6 quad_perm:[2,3,0,1] row_mask:0xf bank_mask:0xf
	s_nop 1
	v_mov_b32_e32 v7, v6
	s_nop 1
	v_add_f32_dpp v6, v7, v6 row_shl:4 row_mask:0xf bank_mask:0x5
	s_nop 1
	v_add_f32_dpp v6, v7, v6 row_shr:4 row_mask:0xf bank_mask:0xa
	s_nop 1
	v_mov_b32_e32 v7, 0
	s_waitcnt lgkmcnt(0)
	v_add_f32_e32 v6, v6, v7
	v_mov_b32_e32 v7, 0
	s_waitcnt lgkmcnt(0)
	v_add_f32_e32 v6, v6, v7
	v_mov_b32_e32 v7, 0
	s_and_saveexec_b64 s[20:21], vcc
	s_cbranch_execz .LBB0_486
	s_waitcnt lgkmcnt(0)
	v_add_f32_e32 v6, v6, v7
	ds_write_b32 v103, v6 offset:3584
.LBB0_486:
	s_or_b64 exec, exec, s[20:21]
	v_and_b32_e32 v10, 0xffff0000, v2
	v_and_b32_e32 v12, 0xffff0000, v3
	v_lshlrev_b32_e32 v11, 16, v2
	v_mul_f32_e32 v2, v10, v10
	v_lshlrev_b32_e32 v13, 16, v3
	v_mul_f32_e32 v3, v12, v12
	v_fmac_f32_e32 v2, v11, v11
	v_fmac_f32_e32 v3, v13, v13
	v_and_b32_e32 v14, 0xffff0000, v4
	v_add_f32_e32 v2, v2, v3
	v_lshlrev_b32_e32 v15, 16, v4
	v_mul_f32_e32 v3, v14, v14
	v_fmac_f32_e32 v3, v15, v15
	v_and_b32_e32 v16, 0xffff0000, v5
	v_add_f32_e32 v2, v3, v2
	v_lshlrev_b32_e32 v17, 16, v5
	v_mul_f32_e32 v3, v16, v16
	v_fmac_f32_e32 v3, v17, v17
	v_add_f32_e32 v2, v3, v2
	s_nop 1
	v_add_f32_dpp v2, v2, v2 quad_perm:[1,0,3,2] row_mask:0xf bank_mask:0xf
	s_nop 1
	v_add_f32_dpp v2, v2, v2 quad_perm:[2,3,0,1] row_mask:0xf bank_mask:0xf
	s_nop 1
	v_mov_b32_e32 v3, v2
	s_nop 1
	v_add_f32_dpp v2, v3, v2 row_shl:4 row_mask:0xf bank_mask:0x5
	s_nop 1
	v_add_f32_dpp v2, v3, v2 row_shr:4 row_mask:0xf bank_mask:0xa
	s_nop 1
	v_mov_b32_e32 v3, 0
	s_waitcnt lgkmcnt(0)
	v_add_f32_e32 v2, v2, v3
	v_mov_b32_e32 v3, 0
	s_waitcnt lgkmcnt(0)
	v_add_f32_e32 v2, v2, v3
	v_mov_b32_e32 v3, 0
	s_and_saveexec_b64 s[20:21], vcc
	s_cbranch_execz .LBB0_488
	s_waitcnt lgkmcnt(0)
	v_add_f32_e32 v2, v2, v3
	ds_write_b32 v103, v2 offset:3840
